# attention: one static s_setprio 1 for the younger wave half (waves 4-7, MLA items), reset at phase exit
# baseline (speedup 1.0000x reference)
; #define LDS_AS __attribute__((address_space(3)))
; DI void attn_step_end() { asm volatile("s_waitcnt vmcnt(0)" ::: "memory"); __builtin_amdgcn_s_barrier(); }
; DI void attn_step_end_ml() { asm volatile("s_waitcnt vmcnt(4)" ::: "memory"); __builtin_amdgcn_s_barrier(); }
; DI void attn_mla_item(const Params& p, LDS_AS unsigned char* lds, const AttnCtx& c, int qb, int nsteps) {
;   const int lane = c.lane, l31 = lane & 31, hh = lane >> 5;
;   const size_t tokbase = (size_t)c.b * SEQ;
;   bf16x8 qf[12];
;   {
;     const bf16_t* qp = p.mq + (tokbase + qb * 32 + l31) * 1536 + c.hd * 192 + 8 * hh;
; #pragma unroll
;     for (int s = 0; s < 12; ++s) qf[s] = *(const bf16x8*)(qp + 16 * s);
;   }
;   f32x16 o[4];
; #pragma unroll
;   for (int d = 0; d < 4; ++d)
; #pragma unroll
;     for (int i = 0; i < 16; ++i) o[d][i] = 0.f;
;   float mrun = -1e30f, lrun = 0.f;
;   attn_issue(c, nsteps - 1, 0);
;   attn_issue(c, nsteps - 2, 1);
;   attn_step_end_ml();
;   int s = 0, rb = 0;
;   const int nskip = nsteps - ((qb >> 1) + 1) * 2;
; #pragma unroll 1
;   for (; s < nskip; ++s) { if (s + 2 < nsteps) { attn_issue(c, nsteps - 3 - s, rb == 0 ? 2 : rb - 1); attn_step_end_ml(); } else attn_step_end(); rb = rb == 2 ? 0 : rb + 1; }
; DI void phase_attn(const Params& p, LDS_AS unsigned char* lds, char* smem, int bid, int nb) {
;     ...
; #pragma unroll 1
;   for (int rnd = 0; rnd * nb < 512; ++rnd) {
;     const int s = __builtin_amdgcn_readfirstlane(rnd * nb + ((rnd & 1) ? nb - 1 - bid : bid));
;     if (s >= 512) break;
;     const int q8 = ((rnd & 1) && (nb & 7) == 0) ? 7 - (s & 7) : (s & 7);
;     const int bh = q8 * 4 + ((s >> 3) & 3), ch = 15 - (s >> 5);
;     c.b = bh >> 3; c.hd = bh & 7;
;     c.voff_sbk = drow * 6144u + (unsigned)(1024 + c.hd * 128) * 2u + dch * 16u;
;     c.voff_sbv = drow * 6144u + (unsigned)(2048 + c.hd * 128) * 2u + dch * 16u;
;     c.voff_mlk = drow * 4096u + (unsigned)(c.hd * 256) * 2u + dch * 16u;
;     c.voff_mlv = drow * 4096u + (unsigned)(c.hd * 256 + 128) * 2u + dch * 16u;
;     c.voff_r = rrow * 128u + rch * 16u;
;     if (c.wv < 4) attn_sb_item(p, lds, c, 4 * ch + w4, 4 * ch + 4);
;     else attn_mla_item(p, lds, c, 4 * ch + w4, 4 * ch + 4);
.LBB0_1016:
	s_bitcmp1_b32 s49, 0
	s_cselect_b64 s[84:85], -1, 0
	s_and_b64 s[38:39], s[84:85], exec
	v_readlane_b32 s4, v255, 17
	v_readlane_b32 s5, v255, 21
	s_cselect_b32 s33, s5, s4
	s_add_i32 s33, s33, s0
	s_cmpk_gt_i32 s33, 0x1ff
	s_mov_b64 s[78:79], -1
	s_cbranch_scc1 .LBB0_1015
	v_readlane_b32 s4, v255, 23
	v_readlane_b32 s5, v255, 24
	s_and_b32 s0, s33, 7
	s_and_b64 s[38:39], s[4:5], s[84:85]
	s_xor_b32 s42, s0, 7
	s_and_b64 s[38:39], s[38:39], exec
	s_cselect_b32 s38, s42, s0
	s_ashr_i32 s42, s33, 3
	s_lshl_b32 s0, s38, 2
	s_bfe_u32 s39, s33, 0x20003
	s_and_b32 s33, s42, -4
	s_and_b32 s0, s0, 4
	s_sub_i32 s43, 60, s33
	v_readlane_b32 s4, v255, 30
	s_or_b32 s76, s0, s39
	s_or_b32 s39, s43, s4
	s_lshl_b32 s38, s38, 10
	s_and_b32 s55, s38, 0x1800
	s_lshl_b32 s38, s39, 5
	v_readlane_b32 s4, v255, 25
	s_lshl_b32 s0, s76, 8
	v_lshl_add_u32 v168, s76, 9, v165
	s_add_i32 s38, s55, s38
	v_readlane_b32 s5, v255, 26
	v_add_u32_e32 v166, s0, v136
	v_add_u32_e32 v167, s0, v137
	v_or_b32_e32 v169, 0x100, v168
	s_sub_i32 s33, 64, s33
	v_or_b32_e32 v132, s38, v139
	v_mov_b32_e32 v133, v0
	s_and_b64 vcc, exec, s[4:5]
	s_cbranch_vccz .LBB0_1039
	s_setprio 1
	v_readlane_b32 s4, v254, 56
	v_readlane_b32 s18, v255, 6
	v_readlane_b32 s19, v255, 7
	s_movk_i32 s38, 0xc00
	v_mov_b32_e32 v131, v0
	v_mov_b64_e32 v[2:3], s[18:19]
	v_mad_u64_u32 v[2:3], s[62:63], v132, s38, v[2:3]
	s_mul_i32 s62, s76, 0x180
	s_mov_b32 s63, s1
	v_lshl_add_u64 v[2:3], v[2:3], 0, s[62:63]
	v_lshl_add_u64 v[2:3], v[2:3], 0, v[130:131]
	global_load_dwordx4 v[82:85], v[2:3], off
	global_load_dwordx4 v[86:89], v[2:3], off offset:32
	global_load_dwordx4 v[90:93], v[2:3], off offset:64
	global_load_dwordx4 v[94:97], v[2:3], off offset:96
	global_load_dwordx4 v[98:101], v[2:3], off offset:128
	global_load_dwordx4 v[102:105], v[2:3], off offset:160
	global_load_dwordx4 v[106:109], v[2:3], off offset:192
	global_load_dwordx4 v[110:113], v[2:3], off offset:224
	global_load_dwordx4 v[114:117], v[2:3], off offset:256
	global_load_dwordx4 v[118:121], v[2:3], off offset:288
	global_load_dwordx4 v[122:125], v[2:3], off offset:320
	global_load_dwordx4 v[126:129], v[2:3], off offset:352
	s_lshl_b32 s38, s43, 5
	s_add_i32 s38, s55, s38
	s_addk_i32 s38, 0x60
	s_mul_i32 s46, s38, 0x1800
	s_mov_b32 m0, s77
	s_nop 0
	buffer_load_dwordx4 v166, s[64:67], s46 offen lds
	s_lshl_b32 s38, s38, 12
	s_mov_b32 m0, s72
	s_nop 0
	buffer_load_dwordx4 v167, s[64:67], s46 offen lds
	v_readlane_b32 s4, v255, 27
	s_mov_b32 m0, s73
	s_nop 0
	buffer_load_dwordx4 v168, s[68:71], s38 offen lds
	s_mov_b32 s61, 0
	s_mov_b32 m0, s74
	s_nop 0
	buffer_load_dwordx4 v169, s[68:71], s38 offen lds
	s_lshl_b32 s38, s33, 5
	s_add_i32 s38, s55, s38
	s_sub_i32 s38, s38, 64
	s_mul_i32 s46, s38, 0x1800
	s_mov_b32 m0, s75
	s_nop 0
	buffer_load_dwordx4 v166, s[64:67], s46 offen lds
	s_lshl_b32 s38, s38, 12
	s_mov_b32 m0, s86
	s_nop 0
	buffer_load_dwordx4 v167, s[64:67], s46 offen lds
	s_mov_b32 s46, 0
	s_mov_b32 m0, s87
	s_nop 0
	buffer_load_dwordx4 v168, s[68:71], s38 offen lds
	v_readlane_b32 s5, v254, 57
	s_mov_b32 m0, s4
	s_nop 0
	buffer_load_dwordx4 v169, s[68:71], s38 offen lds
	s_waitcnt vmcnt(4)
	s_and_b32 s38, s39, 0x1ffffffe
	s_sub_i32 s62, s33, s38
	s_or_b32 s39, s43, 2
	s_cmp_lt_i32 s62, 3
	v_readlane_b32 s6, v254, 58
	v_readlane_b32 s7, v254, 59
	v_readlane_b32 s8, v254, 60
	v_readlane_b32 s9, v254, 61
	v_readlane_b32 s10, v254, 62
	v_readlane_b32 s11, v254, 63
	v_readlane_b32 s12, v255, 0
	v_readlane_b32 s13, v255, 1
	v_readlane_b32 s14, v255, 2
	v_readlane_b32 s15, v255, 3
	v_readlane_b32 s16, v255, 4
	v_readlane_b32 s17, v255, 5
	s_barrier
	s_cbranch_scc1 .LBB0_1025
	s_lshl_b32 s38, s42, 5
	s_and_b32 s38, s38, 0xffffff80
	s_sub_i32 s38, s55, s38
	s_addk_i32 s38, 0x7a0
	s_add_i32 s62, s62, -2
	s_mul_i32 s63, s38, 0x1800
	s_lshl_b32 s84, s38, 12
	s_branch .LBB0_1021

; __device__ __forceinline__ unsigned xb_ld(unsigned* p)              { return __hip_atomic_load(p, __ATOMIC_RELAXED, __HIP_MEMORY_SCOPE_AGENT); }
; __device__ __forceinline__ void xcd_barrier_complete(unsigned* bar, unsigned x, unsigned G, unsigned& nloc, unsigned& nx) {
;     unsigned sum, cnt, mine, sp = 0u;
;     for (;;) {
;         sum = 0u; cnt = 0u; mine = 0u;
; #pragma unroll
;         for (unsigned j = 0; j < 16; ++j) { const unsigned c = xb_ld(&bar[XB_XCNT(j)]); sum += c; cnt += (c > 0u) ? 1u : 0u; mine = (j == x) ? c : mine; }
; __device__ __forceinline__ void xcd_barrier(const XcdBarrier& b) {
;     asm volatile("s_waitcnt vmcnt(0)" ::: "memory");
;     __syncthreads();
;     if (threadIdx.x == 0) {
;         unsigned* bar = b.bar;
;         __builtin_amdgcn_s_waitcnt(0);
;         unsigned nloc = b.st[0], nx = b.st[1];
;         if (nloc == 0u) { xcd_barrier_complete(bar, b.x, b.G, nloc, nx); b.st[0] = nloc; b.st[1] = nx; }
; __global__ void __launch_bounds__(NTHREADS, 2) k_forward(Params p_in) {
;     ...
;     if (cbid < nca) phase_attn(p, lds, smem, cbid, nca);
;     xcd_barrier(barc);
.LBB0_1064:
	s_setprio 0
	s_waitcnt vmcnt(0)
	s_waitcnt vmcnt(63) expcnt(7) lgkmcnt(15)
	s_barrier
	s_and_saveexec_b64 s[0:1], s[42:43]
	v_readlane_b32 s56, v255, 10
	v_readlane_b32 s87, v255, 12
	v_readlane_b32 s57, v255, 11
	v_readlane_b32 s54, v254, 52
	v_readlane_b32 s55, v255, 18
	s_cbranch_execz .LBB0_1116
	v_mov_b32_e32 v0, 0
	s_waitcnt vmcnt(0) expcnt(0) lgkmcnt(0)
	ds_read_b32 v2, v0 offset:8
	ds_read_b32 v1, v0 offset:12
	s_waitcnt lgkmcnt(1)
	v_cmp_ne_u32_e32 vcc, 0, v2
	s_cbranch_vccnz .LBB0_1080
	v_readlane_b32 s36, v254, 35
	v_readlane_b32 s37, v254, 36
	s_add_u32 s2, s36, 0x3800
	s_addc_u32 s3, s37, 0
	s_add_u32 s4, s36, 0x3a00
	s_addc_u32 s5, s37, 0
	s_add_u32 s6, s36, 0x3b00
	s_addc_u32 s7, s37, 0
	s_add_u32 s8, s36, 0x3c00
	s_addc_u32 s9, s37, 0
	s_add_u32 s10, s36, 0x3d00
	s_addc_u32 s11, s37, 0
	s_add_u32 s12, s36, 0x3e00
	s_addc_u32 s13, s37, 0
	s_add_u32 s14, s36, 0x3f00
	s_addc_u32 s15, s37, 0
	s_add_u32 s16, s36, 0x4000
	s_addc_u32 s17, s37, 0
	s_add_u32 s18, s36, 0x4100
	s_addc_u32 s19, s37, 0
	s_add_u32 s20, s36, 0x4200
	s_addc_u32 s21, s37, 0
	s_add_u32 s22, s36, 0x4300
	s_addc_u32 s23, s37, 0
	s_add_u32 s24, s36, 0x4400
	s_addc_u32 s25, s37, 0
	s_add_u32 s26, s36, 0x4500
	s_addc_u32 s27, s37, 0
	s_add_u32 s28, s36, 0x4600
	s_addc_u32 s29, s37, 0
	s_add_u32 s30, s36, 0x4700
	s_addc_u32 s31, s37, 0
	s_add_u32 s34, s36, 0x4800
	s_addc_u32 s35, s37, 0
	s_add_u32 s36, s36, 0x4900
	s_addc_u32 s37, s37, 0
	s_mov_b32 s33, 1
	v_readlane_b32 s38, v254, 37
	v_readlane_b32 s39, v254, 38
	s_branch .LBB0_1068
